# weight prep: the per-layer-embedding weight transpose loop issues its 16 row loads up front with counted waits (was 8 serialized two-load round trips per iteration)
# speedup vs baseline: 1.0028x; 1.0028x over previous
;     const int nblk = ncols / 32, kb = item / nblk, nb = item % nblk, k0 = 64 * kb, n0 = 32 * nb;
; #pragma unroll 8
;     for (int i = 0; i < 32; ++i) { const int kk = 2 * i + (lane >> 5); scr[kk * 33 + (lane & 31)] = W[(size_t)(k0 + kk) * ldw + n0 + (lane & 31)]; }
;     asm volatile("s_waitcnt lgkmcnt(0)" ::: "memory");
.LBB0_1217:
	s_lshl_b32 s39, s37, 1
	s_lshl_b32 s48, s30, 1
	v_add_u32_e32 v86, s39, v64
	v_add_u32_e32 v84, s48, v55
	v_ashrrev_i32_e32 v87, 31, v86
	v_ashrrev_i32_e32 v85, 31, v84
	v_lshlrev_b64 v[86:87], 12, v[86:87]
	v_lshlrev_b64 v[84:85], 12, v[84:85]
	v_lshl_add_u64 v[86:87], v[62:63], 0, v[86:87]
	v_lshl_add_u64 v[84:85], v[62:63], 0, v[84:85]
	global_load_dword v100, v[86:87], off
	global_load_dword v101, v[84:85], off
	v_add_u32_e32 v88, s48, v1
	v_add_u32_e32 v89, s39, v26
	v_mad_u64_u32 v[116:117], s[52:53], v89, s26, v[28:29]
	v_mad_u64_u32 v[118:119], s[52:53], v88, s26, v[28:29]
	v_add_u32_e32 v88, s48, v3
	v_add_u32_e32 v89, s39, v48
	s_add_i32 s37, s37, 16
	s_add_i32 s30, s30, 16
	s_add_i32 s38, s38, -16
	s_cmp_eq_u32 s38, 0
	v_add_u32_e32 v86, s39, v66
	v_add_u32_e32 v84, s48, v57
	v_ashrrev_i32_e32 v87, 31, v86
	v_ashrrev_i32_e32 v85, 31, v84
	v_lshlrev_b64 v[86:87], 12, v[86:87]
	v_lshlrev_b64 v[84:85], 12, v[84:85]
	v_lshl_add_u64 v[86:87], v[62:63], 0, v[86:87]
	v_lshl_add_u64 v[84:85], v[62:63], 0, v[84:85]
	global_load_dword v102, v[86:87], off
	global_load_dword v103, v[84:85], off
	v_mad_u64_u32 v[120:121], s[52:53], v89, s26, v[28:29]
	v_mad_u64_u32 v[122:123], s[52:53], v88, s26, v[28:29]
	v_add_u32_e32 v88, s48, v27
	v_add_u32_e32 v89, s39, v50
	v_add_u32_e32 v86, s39, v68
	v_add_u32_e32 v84, s48, v59
	v_ashrrev_i32_e32 v87, 31, v86
	v_ashrrev_i32_e32 v85, 31, v84
	v_lshlrev_b64 v[86:87], 12, v[86:87]
	v_lshlrev_b64 v[84:85], 12, v[84:85]
	v_lshl_add_u64 v[86:87], v[62:63], 0, v[86:87]
	v_lshl_add_u64 v[84:85], v[62:63], 0, v[84:85]
	global_load_dword v104, v[86:87], off
	global_load_dword v105, v[84:85], off
	v_mad_u64_u32 v[124:125], s[52:53], v89, s26, v[28:29]
	v_mad_u64_u32 v[126:127], s[52:53], v88, s26, v[28:29]
	v_add_u32_e32 v88, s48, v29
	v_add_u32_e32 v89, s39, v52
	v_add_u32_e32 v86, s39, v70
	v_add_u32_e32 v84, s48, v61
	v_ashrrev_i32_e32 v87, 31, v86
	v_ashrrev_i32_e32 v85, 31, v84
	v_lshlrev_b64 v[86:87], 12, v[86:87]
	v_lshlrev_b64 v[84:85], 12, v[84:85]
	v_lshl_add_u64 v[86:87], v[62:63], 0, v[86:87]
	v_lshl_add_u64 v[84:85], v[62:63], 0, v[84:85]
	global_load_dword v106, v[86:87], off
	global_load_dword v107, v[84:85], off
	v_mad_u64_u32 v[128:129], s[52:53], v89, s26, v[28:29]
	v_mad_u64_u32 v[130:131], s[52:53], v88, s26, v[28:29]
	v_add_u32_e32 v88, s48, v31
	v_add_u32_e32 v89, s39, v54
	v_add_u32_e32 v86, s39, v72
	v_add_u32_e32 v84, s48, v65
	v_ashrrev_i32_e32 v87, 31, v86
	v_ashrrev_i32_e32 v85, 31, v84
	v_lshlrev_b64 v[86:87], 12, v[86:87]
	v_lshlrev_b64 v[84:85], 12, v[84:85]
	v_lshl_add_u64 v[86:87], v[62:63], 0, v[86:87]
	v_lshl_add_u64 v[84:85], v[62:63], 0, v[84:85]
	global_load_dword v108, v[86:87], off
	global_load_dword v109, v[84:85], off
	v_mad_u64_u32 v[132:133], s[52:53], v89, s26, v[28:29]
	v_mad_u64_u32 v[134:135], s[52:53], v88, s26, v[28:29]
	v_add_u32_e32 v88, s48, v49
	v_add_u32_e32 v89, s39, v56
	v_add_u32_e32 v86, s39, v74
	v_add_u32_e32 v84, s48, v67
	v_ashrrev_i32_e32 v87, 31, v86
	v_ashrrev_i32_e32 v85, 31, v84
	v_lshlrev_b64 v[86:87], 12, v[86:87]
	v_lshlrev_b64 v[84:85], 12, v[84:85]
	v_lshl_add_u64 v[86:87], v[62:63], 0, v[86:87]
	v_lshl_add_u64 v[84:85], v[62:63], 0, v[84:85]
	global_load_dword v110, v[86:87], off
	global_load_dword v111, v[84:85], off
	v_mad_u64_u32 v[136:137], s[52:53], v89, s26, v[28:29]
	v_mad_u64_u32 v[138:139], s[52:53], v88, s26, v[28:29]
	v_add_u32_e32 v88, s48, v51
	v_add_u32_e32 v89, s39, v58
	v_add_u32_e32 v86, s39, v76
	v_add_u32_e32 v84, s48, v69
	v_ashrrev_i32_e32 v87, 31, v86
	v_ashrrev_i32_e32 v85, 31, v84
	v_lshlrev_b64 v[86:87], 12, v[86:87]
	v_lshlrev_b64 v[84:85], 12, v[84:85]
	v_lshl_add_u64 v[86:87], v[62:63], 0, v[86:87]
	v_lshl_add_u64 v[84:85], v[62:63], 0, v[84:85]
	global_load_dword v112, v[86:87], off
	global_load_dword v113, v[84:85], off
	v_mad_u64_u32 v[140:141], s[52:53], v89, s26, v[28:29]
	v_mad_u64_u32 v[142:143], s[52:53], v88, s26, v[28:29]
	v_add_u32_e32 v89, s39, v60
	v_add_u32_e32 v88, s48, v53
	v_add_u32_e32 v86, s39, v78
	v_add_u32_e32 v84, s48, v71
	v_ashrrev_i32_e32 v87, 31, v86
	v_ashrrev_i32_e32 v85, 31, v84
	v_lshlrev_b64 v[86:87], 12, v[86:87]
	v_lshlrev_b64 v[84:85], 12, v[84:85]
	v_lshl_add_u64 v[86:87], v[62:63], 0, v[86:87]
	v_lshl_add_u64 v[84:85], v[62:63], 0, v[84:85]
	global_load_dword v114, v[86:87], off
	global_load_dword v115, v[84:85], off
	v_mad_u64_u32 v[144:145], s[52:53], v89, s26, v[28:29]
	v_mad_u64_u32 v[146:147], s[52:53], v88, s26, v[28:29]
	s_waitcnt vmcnt(14)
	ds_write_b32 v116, v100
	ds_write_b32 v118, v101
	s_waitcnt vmcnt(12)
	ds_write_b32 v120, v102
	ds_write_b32 v122, v103
	s_waitcnt vmcnt(10)
	ds_write_b32 v124, v104
	ds_write_b32 v126, v105
	s_waitcnt vmcnt(8)
	ds_write_b32 v128, v106
	ds_write_b32 v130, v107
	s_waitcnt vmcnt(6)
	ds_write_b32 v132, v108
	ds_write_b32 v134, v109
	s_waitcnt vmcnt(4)
	ds_write_b32 v136, v110
	ds_write_b32 v138, v111
	s_waitcnt vmcnt(2)
	ds_write_b32 v140, v112
	ds_write_b32 v142, v113
	s_waitcnt vmcnt(0)
	ds_write_b32 v144, v114
	ds_write_b32 v146, v115
	s_cbranch_scc0 .LBB0_1217
